# speedup vs baseline: 1.0112x; 1.0063x over previous
_Z7kfinal3PKDF16_PKfS2_S2_PK15HIP_vector_typeIjLj4EES2_Pf:
	s_load_dwordx2 s[20:21], s[0:1], 0x20
	s_load_dwordx4 s[12:15], s[0:1], 0x0
	s_load_dwordx4 s[16:19], s[0:1], 0x10
	v_lshlrev_b32_e32 v136, 3, v0
	v_and_b32_e32 v137, 63, v0
	v_lshlrev_b32_e32 v137, 2, v137
	v_mov_b32_e32 v138, 0
	v_mov_b32_e32 v139, 0
	s_movk_i32 s28, 0x100
	v_cmp_gt_u32_e64 s[30:31], s28, v0
	s_waitcnt lgkmcnt(0)
	s_and_saveexec_b64 s[32:33], s[30:31]
	s_cbranch_execz .Lgn_nopart
	global_load_dwordx2 v[138:139], v136, s[14:15]
.Lgn_nopart:
	s_or_b64 exec, exec, s[32:33]
	global_load_dword v140, v137, s[16:17]
	global_load_dword v141, v137, s[18:19]
	v_lshrrev_b32_e32 v48, 6, v0
	s_bfe_u32 s24, s2, 0x20003
	s_mul_i32 s3, s24, 0x28800
	v_lshlrev_b32_e32 v118, 10, v48
	v_and_b32_e32 v1, 63, v0
	s_waitcnt lgkmcnt(0)
	s_add_u32 s6, s20, s3
	v_add_u32_e32 v2, 0, v118
	s_addc_u32 s7, s21, 0
	v_mov_b32_e32 v47, 0
	v_lshlrev_b32_e32 v46, 4, v1
	v_accvgpr_write_b32 a72, v2
	v_add_u32_e32 v8, 0xc600, v2
	v_and_b32_e32 v2, 0x1c0, v0
	v_lshl_add_u64 v[4:5], s[6:7], 0, v[46:47]
	v_lshlrev_b32_e32 v2, 4, v2
	v_mov_b32_e32 v3, v47
	v_readfirstlane_b32 s3, v8
	v_lshl_add_u64 v[6:7], v[4:5], 0, v[2:3]
	s_mov_b32 m0, s3
	v_or_b32_e32 v49, 8, v48
	global_load_lds_dwordx4 v[6:7], off
	s_movk_i32 s3, 0x280
	v_cmp_gt_u32_e64 s[4:5], s3, v0
	v_lshlrev_b32_e32 v90, 10, v49
	s_and_saveexec_b64 s[8:9], s[4:5]
	s_cbranch_execz .LBB3_2
	v_add_u32_e32 v3, 0, v90
	v_add_u32_e32 v3, 0xc600, v3
	v_mov_b32_e32 v91, v47
	v_readfirstlane_b32 s3, v3
	v_lshl_add_u64 v[6:7], v[4:5], 0, v[90:91]
	s_mov_b32 m0, s3
	s_nop 0
	global_load_lds_dwordx4 v[6:7], off

.LBB3_8:
	s_or_b64 exec, exec, s[6:7]
	s_lshl_b32 s3, s2, 2
	s_and_b32 s26, s3, 28
	s_lshr_b32 s3, s2, 6
	s_lshl_b32 s2, s2, 1
	s_add_i32 s26, s26, s3
	s_and_b32 s22, s2, 64
	v_lshrrev_b32_e32 v47, 3, v0
	s_movk_i32 s2, 0x20f
	s_lshl_b32 s23, s26, 2
	v_mov_b32_e32 v4, 0xffffffbe
	v_cmp_lt_u32_e64 s[6:7], s2, v0
	v_or_b32_e32 v66, 64, v47
	v_mul_lo_u16_e32 v6, 63, v66
	v_cndmask_b32_e64 v70, 0, v4, s[6:7]
	v_mov_b32_e32 v4, s23
	s_add_i32 s25, s23, -1
	s_add_i32 s27, s22, -1
	v_lshlrev_b32_e32 v28, 3, v0
	v_addc_co_u32_e64 v71, vcc, -1, v4, s[6:7]
	v_mov_b32_e32 v8, 0x7f
	v_lshrrev_b16_e32 v65, 12, v6
	v_and_b32_e32 v30, 56, v28
	v_med3_i32 v4, v71, 0, v8
	v_add3_u32 v5, s27, v47, v70
	v_mul_i32_i24_e32 v68, 0xffffffbe, v65
	v_add_u32_e32 v67, s25, v65
	v_lshlrev_b32_e32 v26, 1, v30
	v_mov_b32_e32 v27, 0
	v_med3_i32 v5, v5, 0, v8
	v_lshlrev_b32_e32 v4, 14, v4
	v_med3_i32 v6, v67, 0, v8
	v_add3_u32 v7, s27, v66, v68
	s_waitcnt lgkmcnt(0)
	v_lshl_add_u64 v[2:3], s[12:13], 0, v[26:27]
	v_lshl_or_b32 v26, v5, 7, v4
	v_med3_i32 v7, v7, 0, v8
	v_lshlrev_b32_e32 v6, 14, v6
	v_lshl_add_u64 v[4:5], v[2:3], 0, v[26:27]
	v_lshl_or_b32 v26, v7, 7, v6
	v_or_b32_e32 v62, 0x80, v47
	v_lshl_add_u64 v[6:7], v[2:3], 0, v[26:27]
	global_load_dwordx4 v[42:45], v[4:5], off
	global_load_dwordx4 v[22:25], v[6:7], off
	v_mul_lo_u16_e32 v4, 0xf9, v62
	v_or_b32_e32 v58, 0xc0, v47
	v_lshrrev_b16_e32 v61, 14, v4
	v_mul_u32_u24_e32 v6, 0x3e1, v58
	v_mul_i32_i24_e32 v64, 0xffffffbe, v61
	v_add_u32_e32 v63, s25, v61
	v_lshrrev_b32_e32 v57, 16, v6
	v_min_u32_e32 v4, 0x7f, v63
	v_add3_u32 v5, s27, v62, v64
	v_mul_i32_i24_e32 v60, 0xffffffbe, v57
	v_add_u32_e32 v59, s25, v57
	v_med3_i32 v5, v5, 0, v8
	v_lshlrev_b32_e32 v4, 14, v4
	v_min_u32_e32 v6, 0x7f, v59
	v_add3_u32 v7, s27, v58, v60
	v_lshl_or_b32 v26, v5, 7, v4
	v_med3_i32 v7, v7, 0, v8
	v_lshlrev_b32_e32 v6, 14, v6
	v_lshl_add_u64 v[4:5], v[2:3], 0, v[26:27]
	v_lshl_or_b32 v26, v7, 7, v6
	v_or_b32_e32 v54, 0x100, v47
	v_lshl_add_u64 v[6:7], v[2:3], 0, v[26:27]
	global_load_dwordx4 v[18:21], v[4:5], off
	global_load_dwordx4 v[14:17], v[6:7], off
	v_mul_u32_u24_e32 v4, 0x3e1, v54
	v_lshrrev_b32_e32 v53, 16, v4
	v_or_b32_e32 v52, 0x140, v47
	s_movk_i32 s3, 0xffbe
	v_mul_i32_i24_e32 v56, 0xffffffbe, v53
	v_add_u32_e32 v55, s25, v53
	v_mul_u32_u24_e32 v6, 0x3e1, v52
	v_min_u32_e32 v4, 0x7f, v55
	v_add3_u32 v5, s27, v54, v56
	v_mul_i32_i24_sdwa v7, v6, s3 dst_sel:DWORD dst_unused:UNUSED_PAD src0_sel:WORD_1 src1_sel:DWORD
	v_add_u32_sdwa v6, s25, v6 dst_sel:DWORD dst_unused:UNUSED_PAD src0_sel:DWORD src1_sel:WORD_1
	v_med3_i32 v5, v5, 0, v8
	v_lshlrev_b32_e32 v4, 14, v4
	v_min_u32_e32 v6, 0x7f, v6
	v_add3_u32 v7, s27, v52, v7
	v_lshl_or_b32 v26, v5, 7, v4
	v_med3_i32 v7, v7, 0, v8
	v_lshlrev_b32_e32 v6, 14, v6
	v_lshl_add_u64 v[4:5], v[2:3], 0, v[26:27]
	v_lshl_or_b32 v26, v7, 7, v6
	v_or_b32_e32 v51, 0x180, v47
	v_lshl_add_u64 v[32:33], v[2:3], 0, v[26:27]
	global_load_dwordx4 v[10:13], v[4:5], off
	global_load_dwordx4 v[6:9], v[32:33], off
	v_min_u32_e32 v4, 0x18b, v51
	s_min_u32 s2, s23, 0x7b
	v_add_u32_e32 v4, s27, v4
	v_add_u32_e32 v4, 0xfffffeb6, v4
	s_lshl_b32 s2, s2, 14
	v_min_u32_e32 v4, 0x7f, v4
	s_add_i32 s2, s2, 0x10000
	v_lshl_or_b32 v26, v4, 7, s2
	v_lshl_add_u64 v[2:3], v[2:3], 0, v[26:27]
	global_load_dwordx4 v[2:5], v[2:3], off
	s_movk_i32 s38, 0xff94
	s_movk_i32 s39, 0xffee
	s_add_i32 s40, s22, -4
	v_mov_b32_e32 v131, 0x7f
	v_mov_b32_e32 v132, 0x7c
	v_min_u32_e32 v133, 27, v50
	v_min_u32_e32 v134, 3, v48
	v_or_b32_e32 v134, 24, v134
	v_lshl_or_b32 v128, v48, 6, v1
	v_mul_u32_u24_e32 v129, 0x25f, v128
	v_lshrrev_b32_e32 v129, 16, v129
	v_mad_i32_i24 v128, v129, s38, v128
	v_mul_u32_u24_e32 v130, 0xe39, v128
	v_lshrrev_b32_e32 v130, 16, v130
	v_mad_i32_i24 v128, v130, s39, v128
	v_add_u32_e32 v130, s25, v130
	v_med3_i32 v130, v130, 0, v131
	v_lshl_add_u32 v128, v128, 2, s40
	v_med3_i32 v128, v128, 0, v132
	v_min_u32_e32 v129, 15, v129
	v_lshlrev_b32_e32 v129, 14, v129
	v_lshlrev_b32_e32 v130, 7, v130
	v_or3_b32 v94, v130, v129, v128
	v_lshl_or_b32 v128, v49, 6, v1
	v_mul_u32_u24_e32 v129, 0x25f, v128
	v_lshrrev_b32_e32 v129, 16, v129
	v_mad_i32_i24 v128, v129, s38, v128
	v_mul_u32_u24_e32 v130, 0xe39, v128
	v_lshrrev_b32_e32 v130, 16, v130
	v_mad_i32_i24 v128, v130, s39, v128
	v_add_u32_e32 v130, s25, v130
	v_med3_i32 v130, v130, 0, v131
	v_lshl_add_u32 v128, v128, 2, s40
	v_med3_i32 v128, v128, 0, v132
	v_min_u32_e32 v129, 15, v129
	v_lshlrev_b32_e32 v129, 14, v129
	v_lshlrev_b32_e32 v130, 7, v130
	v_or3_b32 v96, v130, v129, v128
	v_lshl_or_b32 v128, v133, 6, v1
	v_mul_u32_u24_e32 v129, 0x25f, v128
	v_lshrrev_b32_e32 v129, 16, v129
	v_mad_i32_i24 v128, v129, s38, v128
	v_mul_u32_u24_e32 v130, 0xe39, v128
	v_lshrrev_b32_e32 v130, 16, v130
	v_mad_i32_i24 v128, v130, s39, v128
	v_add_u32_e32 v130, s25, v130
	v_med3_i32 v130, v130, 0, v131
	v_lshl_add_u32 v128, v128, 2, s40
	v_med3_i32 v128, v128, 0, v132
	v_min_u32_e32 v129, 15, v129
	v_lshlrev_b32_e32 v129, 14, v129
	v_lshlrev_b32_e32 v130, 7, v130
	v_or3_b32 v98, v130, v129, v128
	v_lshl_or_b32 v128, v134, 6, v1
	v_mul_u32_u24_e32 v129, 0x25f, v128
	v_lshrrev_b32_e32 v129, 16, v129
	v_mad_i32_i24 v128, v129, s38, v128
	v_mul_u32_u24_e32 v130, 0xe39, v128
	v_lshrrev_b32_e32 v130, 16, v130
	v_mad_i32_i24 v128, v130, s39, v128
	v_add_u32_e32 v130, s25, v130
	v_med3_i32 v130, v130, 0, v131
	v_lshl_add_u32 v128, v128, 2, s40
	v_med3_i32 v128, v128, 0, v132
	v_min_u32_e32 v129, 15, v129
	v_lshlrev_b32_e32 v129, 14, v129
	v_lshlrev_b32_e32 v130, 7, v130
	v_or3_b32 v100, v130, v129, v128
	v_cmp_eq_u32_e32 vcc, 27, v134
	v_readfirstlane_b32 s41, v100
	s_nop 1
	v_mov_b32_e32 v135, s41
	v_cndmask_b32_e32 v100, v100, v135, vcc
	v_accvgpr_write_b32 a3, 0
	v_accvgpr_write_b32 a2, 0
	v_accvgpr_write_b32 a1, 0
	v_accvgpr_write_b32 a0, 0
	v_accvgpr_write_b32 a7, 0
	v_accvgpr_write_b32 a6, 0
	v_accvgpr_write_b32 a5, 0
	v_accvgpr_write_b32 a4, 0
	v_accvgpr_write_b32 a15, 0
	v_accvgpr_write_b32 a14, 0
	v_accvgpr_write_b32 a13, 0
	v_accvgpr_write_b32 a12, 0
	v_accvgpr_write_b32 a19, 0
	v_accvgpr_write_b32 a18, 0
	v_accvgpr_write_b32 a17, 0
	v_accvgpr_write_b32 a16, 0
	v_accvgpr_write_b32 a31, 0
	v_accvgpr_write_b32 a30, 0
	v_accvgpr_write_b32 a29, 0
	v_accvgpr_write_b32 a28, 0
	v_accvgpr_write_b32 a63, 0
	v_accvgpr_write_b32 a62, 0
	v_accvgpr_write_b32 a61, 0
	v_accvgpr_write_b32 a60, 0
	v_accvgpr_write_b32 a11, 0
	v_accvgpr_write_b32 a10, 0
	v_accvgpr_write_b32 a9, 0
	v_accvgpr_write_b32 a8, 0
	v_accvgpr_write_b32 a23, 0
	v_accvgpr_write_b32 a22, 0
	v_accvgpr_write_b32 a21, 0
	v_accvgpr_write_b32 a20, 0
	v_accvgpr_write_b32 a27, 0
	v_accvgpr_write_b32 a26, 0
	v_accvgpr_write_b32 a25, 0
	v_accvgpr_write_b32 a24, 0
	v_accvgpr_write_b32 a39, 0
	v_accvgpr_write_b32 a38, 0
	v_accvgpr_write_b32 a37, 0
	v_accvgpr_write_b32 a36, 0
	v_accvgpr_write_b32 a47, 0
	v_accvgpr_write_b32 a46, 0
	v_accvgpr_write_b32 a45, 0
	v_accvgpr_write_b32 a44, 0
	v_accvgpr_write_b32 a67, 0
	v_accvgpr_write_b32 a66, 0
	v_accvgpr_write_b32 a65, 0
	v_accvgpr_write_b32 a64, 0
	v_accvgpr_write_b32 a35, 0
	v_accvgpr_write_b32 a34, 0
	v_accvgpr_write_b32 a33, 0
	v_accvgpr_write_b32 a32, 0
	v_accvgpr_write_b32 a43, 0
	v_accvgpr_write_b32 a42, 0
	v_accvgpr_write_b32 a41, 0
	v_accvgpr_write_b32 a40, 0
	v_accvgpr_write_b32 a51, 0
	v_accvgpr_write_b32 a50, 0
	v_accvgpr_write_b32 a49, 0
	v_accvgpr_write_b32 a48, 0
	v_accvgpr_write_b32 a55, 0
	v_accvgpr_write_b32 a54, 0
	v_accvgpr_write_b32 a53, 0
	v_accvgpr_write_b32 a52, 0
	v_accvgpr_write_b32 a59, 0
	v_accvgpr_write_b32 a58, 0
	v_accvgpr_write_b32 a57, 0
	v_accvgpr_write_b32 a56, 0
	v_accvgpr_write_b32 a71, 0
	v_accvgpr_write_b32 a70, 0
	v_accvgpr_write_b32 a69, 0
	v_accvgpr_write_b32 a68, 0
	s_waitcnt vmcnt(11)
	v_mov_b32_dpp v28, v138 row_shr:1 row_mask:0xf bank_mask:0xf bound_ctrl:1
	v_mov_b32_dpp v29, v139 row_shr:1 row_mask:0xf bank_mask:0xf bound_ctrl:1
	v_pk_add_f32 v[26:27], v[138:139], v[28:29]
	v_mov_b32_e32 v34, 0
	v_mov_b32_e32 v35, 0
	v_mov_b32_dpp v28, v26 row_shr:2 row_mask:0xf bank_mask:0xf bound_ctrl:1
	v_mov_b32_dpp v29, v27 row_shr:2 row_mask:0xf bank_mask:0xf bound_ctrl:1
	v_pk_add_f32 v[26:27], v[26:27], v[28:29]
	v_cmp_eq_u32_e32 vcc, 63, v1
	s_nop 0
	v_mov_b32_dpp v28, v26 row_shr:4 row_mask:0xf bank_mask:0xf bound_ctrl:1
	v_mov_b32_dpp v29, v27 row_shr:4 row_mask:0xf bank_mask:0xf bound_ctrl:1
	v_pk_add_f32 v[26:27], v[26:27], v[28:29]
	s_nop 1
	v_mov_b32_dpp v28, v26 row_shr:8 row_mask:0xf bank_mask:0xf bound_ctrl:1
	v_mov_b32_dpp v29, v27 row_shr:8 row_mask:0xf bank_mask:0xf bound_ctrl:1
	v_pk_add_f32 v[28:29], v[26:27], v[28:29]
	v_mov_b32_e32 v27, 0
	v_mov_b32_e32 v26, 0
	v_mov_b32_dpp v34, v28 row_bcast:15 row_mask:0xa bank_mask:0xf
	v_mov_b32_dpp v35, v29 row_bcast:15 row_mask:0xa bank_mask:0xf
	v_pk_add_f32 v[28:29], v[28:29], v[34:35]
	s_nop 1
	v_mov_b32_dpp v26, v28 row_bcast:31 row_mask:0xc bank_mask:0xf
	v_mov_b32_dpp v27, v29 row_bcast:31 row_mask:0xc bank_mask:0xf
	s_and_saveexec_b64 s[2:3], vcc
	v_lshl_add_u32 v33, v48, 3, 0
	v_add_u32_e32 v33, 0x15800, v33
	v_pk_add_f32 v[26:27], v[28:29], v[26:27]
	ds_write_b64 v33, v[26:27]
	s_or_b64 exec, exec, s[2:3]
	v_cmp_gt_u32_e32 vcc, 64, v0
	s_waitcnt lgkmcnt(0)
	s_barrier
	s_and_saveexec_b64 s[10:11], vcc
	s_cbranch_execz .LBB3_16
	s_add_i32 s2, 0, 0x15800
	v_mov_b32_e32 v26, s2
	s_add_i32 s2, 0, 0x15810
	v_mov_b32_e32 v33, s2
	ds_read_b128 v[26:29], v26
	ds_read_b128 v[34:37], v33
	s_mov_b32 s2, 0xf800000
	s_waitcnt lgkmcnt(1)
	v_add_f32_e32 v26, v26, v28
	s_waitcnt lgkmcnt(0)
	v_add_f32_e32 v28, v34, v36
	v_add_f32_e32 v26, v26, v28
	v_add_f32_e32 v27, v27, v29
	v_add_f32_e32 v28, v35, v37
	v_add_f32_e32 v27, v27, v28
	v_mul_f32_e32 v26, 0x35800000, v26
	v_mul_f32_e32 v27, 0x35800000, v27
	v_fma_f32 v27, -v26, v26, v27
	v_add_f32_e32 v27, 0x3727c5ac, v27
	v_mul_f32_e32 v28, 0x4f800000, v27
	v_cmp_gt_f32_e32 vcc, s2, v27
	s_nop 1
	v_cndmask_b32_e32 v27, v27, v28, vcc
	v_sqrt_f32_e32 v28, v27
	s_nop 0
	v_add_u32_e32 v29, -1, v28
	v_fma_f32 v33, -v29, v28, v27
	v_cmp_ge_f32_e64 s[2:3], 0, v33
	v_add_u32_e32 v33, 1, v28
	s_nop 0
	v_cndmask_b32_e64 v29, v28, v29, s[2:3]
	v_fma_f32 v28, -v33, v28, v27
	v_cmp_lt_f32_e64 s[2:3], 0, v28
	s_nop 1
	v_cndmask_b32_e64 v28, v29, v33, s[2:3]
	v_mul_f32_e32 v29, 0x37800000, v28
	v_cndmask_b32_e32 v28, v28, v29, vcc
	v_mov_b32_e32 v29, 0x260
	v_cmp_class_f32_e32 vcc, v27, v29
	s_nop 1
	v_cndmask_b32_e32 v27, v28, v27, vcc
	v_div_scale_f32 v28, s[2:3], v27, v27, 1.0
	v_rcp_f32_e32 v29, v28
	s_nop 0
	v_fma_f32 v33, -v28, v29, 1.0
	v_fmac_f32_e32 v29, v33, v29
	v_div_scale_f32 v33, vcc, 1.0, v27, 1.0
	v_mul_f32_e32 v34, v33, v29
	v_fma_f32 v35, -v28, v34, v33
	v_fmac_f32_e32 v34, v35, v29
	v_fma_f32 v28, -v28, v34, v33
	v_div_fmas_f32 v28, v28, v29, v34
	v_div_fixup_f32 v27, v28, v27, 1.0
	v_lshl_add_u32 v28, v0, 2, 0
	v_mul_f32_e32 v27, v140, v27
	v_add_u32_e32 v29, 0x15600, v28
	ds_write_b32 v29, v27
	v_fma_f32 v26, -v26, v27, v141
	v_add_u32_e32 v27, 0x15700, v28
	ds_write_b32 v27, v26
.LBB3_16:
	s_or_b64 exec, exec, s[10:11]
	v_lshlrev_b32_e32 v34, 2, v30
	s_add_i32 s2, 0, 0x15600
	s_add_i32 s3, 0, 0x15700
	v_add_u32_e32 v26, s2, v34
	v_add_u32_e32 v30, s3, v34
	s_waitcnt lgkmcnt(0)
	s_barrier
	ds_read_b128 v[26:29], v26
	ds_read_b128 v[30:33], v30
	v_or_b32_e32 v34, 16, v34
	s_waitcnt lgkmcnt(0)
	s_waitcnt vmcnt(0)
	v_fma_mixlo_f16 v72, v42, v26, v30 op_sel_hi:[1,0,0]
	v_fma_mixhi_f16 v72, v42, v27, v31 op_sel:[1,0,0] op_sel_hi:[1,0,0]
	v_pk_max_f16 v72, v72, 0
	v_add3_u32 v42, v70, v47, s27
	v_add_u16_e32 v70, v70, v47
	v_add_u32_e32 v35, s2, v34
	v_add_u32_e32 v38, s3, v34
	v_bfe_u32 v69, v0, 3, 1
	v_max_u32_e32 v42, v71, v42
	v_cndmask_b32_e64 v71, 0, 2, s[6:7]
	v_ashrrev_i16_e32 v70, 1, v70
	ds_read_b128 v[34:37], v35
	ds_read_b128 v[38:41], v38
	v_or_b32_e32 v71, v71, v69
	v_bfe_i32 v70, v70, 0, 16
	v_mad_u32_u24 v70, v71, 33, v70
	v_lshlrev_b32_e32 v71, 7, v70
	v_xor_b32_e32 v70, v70, v0
	s_movk_i32 s10, 0x80
	v_lshlrev_b32_e32 v70, 4, v70
	v_cmp_gt_u32_e32 vcc, s10, v42
	v_and_b32_e32 v70, 0x70, v70
	v_fma_mixlo_f16 v73, v43, v28, v32 op_sel_hi:[1,0,0]
	v_fma_mixhi_f16 v73, v43, v29, v33 op_sel:[1,0,0] op_sel_hi:[1,0,0]
	v_pk_max_f16 v73, v73, 0
	s_waitcnt lgkmcnt(0)
	v_fma_mixlo_f16 v74, v44, v34, v38 op_sel_hi:[1,0,0]
	v_fma_mixhi_f16 v74, v44, v35, v39 op_sel:[1,0,0] op_sel_hi:[1,0,0]
	v_pk_max_f16 v74, v74, 0
	v_fma_mixlo_f16 v75, v45, v36, v40 op_sel_hi:[1,0,0]
	v_fma_mixhi_f16 v75, v45, v37, v41 op_sel:[1,0,0] op_sel_hi:[1,0,0]
	v_pk_max_f16 v75, v75, 0
	v_add3_u32 v70, 0, v71, v70
	v_cndmask_b32_e32 v42, 0, v72, vcc
	v_cndmask_b32_e32 v43, 0, v73, vcc
	v_cndmask_b32_e32 v44, 0, v74, vcc
	v_cndmask_b32_e32 v45, 0, v75, vcc
	v_add_u32_e32 v66, v68, v66
	ds_write_b128 v70, v[42:45]
	v_fma_mixlo_f16 v42, v22, v26, v30 op_sel_hi:[1,0,0]
	v_fma_mixhi_f16 v42, v22, v27, v31 op_sel:[1,0,0] op_sel_hi:[1,0,0]
	v_pk_max_f16 v42, v42, 0
	v_add_u32_e32 v22, s27, v66
	v_max_u32_e32 v22, v67, v22
	v_fma_mixlo_f16 v43, v23, v28, v32 op_sel_hi:[1,0,0]
	v_fma_mixhi_f16 v43, v23, v29, v33 op_sel:[1,0,0] op_sel_hi:[1,0,0]
	v_pk_max_f16 v43, v43, 0
	v_cmp_gt_u32_e32 vcc, s10, v22
	v_fma_mixlo_f16 v44, v24, v34, v38 op_sel_hi:[1,0,0]
	v_fma_mixhi_f16 v44, v24, v35, v39 op_sel:[1,0,0] op_sel_hi:[1,0,0]
	v_pk_max_f16 v44, v44, 0
	v_fma_mixlo_f16 v45, v25, v36, v40 op_sel_hi:[1,0,0]
	v_fma_mixhi_f16 v45, v25, v37, v41 op_sel:[1,0,0] op_sel_hi:[1,0,0]
	v_pk_max_f16 v45, v45, 0
	s_load_dwordx2 s[2:3], s[0:1], 0x28
	s_movk_i32 s6, 0x260
	v_cndmask_b32_e32 v22, 0, v42, vcc
	v_cndmask_b32_e32 v23, 0, v43, vcc
	v_lshl_or_b32 v42, v65, 1, v69
	v_ashrrev_i32_e32 v43, 1, v66
	v_mad_u32_u24 v42, v42, 33, v43
	v_lshlrev_b32_e32 v43, 7, v42
	v_xor_b32_e32 v42, v42, v0
	v_lshlrev_b32_e32 v42, 4, v42
	v_and_b32_e32 v42, 0x70, v42
	v_cndmask_b32_e32 v24, 0, v44, vcc
	v_cndmask_b32_e32 v25, 0, v45, vcc
	v_add3_u32 v42, 0, v43, v42
	ds_write_b128 v42, v[22:25]
	v_add_u32_e32 v42, v64, v62
	v_fma_mixlo_f16 v22, v18, v26, v30 op_sel_hi:[1,0,0]
	v_fma_mixhi_f16 v22, v18, v27, v31 op_sel:[1,0,0] op_sel_hi:[1,0,0]
	v_pk_max_f16 v22, v22, 0
	v_add_u32_e32 v18, s27, v42
	v_max_u32_e32 v18, v63, v18
	v_fma_mixlo_f16 v23, v19, v28, v32 op_sel_hi:[1,0,0]
	v_fma_mixhi_f16 v23, v19, v29, v33 op_sel:[1,0,0] op_sel_hi:[1,0,0]
	v_pk_max_f16 v23, v23, 0
	v_cmp_gt_u32_e32 vcc, s10, v18
	v_fma_mixlo_f16 v24, v20, v34, v38 op_sel_hi:[1,0,0]
	v_fma_mixhi_f16 v24, v20, v35, v39 op_sel:[1,0,0] op_sel_hi:[1,0,0]
	v_pk_max_f16 v24, v24, 0
	v_fma_mixlo_f16 v25, v21, v36, v40 op_sel_hi:[1,0,0]
	v_fma_mixhi_f16 v25, v21, v37, v41 op_sel:[1,0,0] op_sel_hi:[1,0,0]
	v_pk_max_f16 v25, v25, 0
	s_nop 1
	v_cndmask_b32_e32 v18, 0, v22, vcc
	v_cndmask_b32_e32 v19, 0, v23, vcc
	v_lshl_or_b32 v22, v61, 1, v69
	v_ashrrev_i32_e32 v23, 1, v42
	v_mad_u32_u24 v22, v22, 33, v23
	v_lshlrev_b32_e32 v23, 7, v22
	v_xor_b32_e32 v22, v22, v0
	v_lshlrev_b32_e32 v22, 4, v22
	v_and_b32_e32 v22, 0x70, v22
	v_cndmask_b32_e32 v20, 0, v24, vcc
	v_cndmask_b32_e32 v21, 0, v25, vcc
	v_add3_u32 v22, 0, v23, v22
	ds_write_b128 v22, v[18:21]
	v_add_u32_e32 v22, v60, v58
	v_fma_mixlo_f16 v18, v14, v26, v30 op_sel_hi:[1,0,0]
	v_fma_mixhi_f16 v18, v14, v27, v31 op_sel:[1,0,0] op_sel_hi:[1,0,0]
	v_pk_max_f16 v18, v18, 0
	v_add_u32_e32 v14, s27, v22
	v_max_u32_e32 v14, v59, v14
	v_fma_mixlo_f16 v19, v15, v28, v32 op_sel_hi:[1,0,0]
	v_fma_mixhi_f16 v19, v15, v29, v33 op_sel:[1,0,0] op_sel_hi:[1,0,0]
	v_pk_max_f16 v19, v19, 0
	v_cmp_gt_u32_e32 vcc, s10, v14
	v_fma_mixlo_f16 v20, v16, v34, v38 op_sel_hi:[1,0,0]
	v_fma_mixhi_f16 v20, v16, v35, v39 op_sel:[1,0,0] op_sel_hi:[1,0,0]
	v_pk_max_f16 v20, v20, 0
	v_fma_mixlo_f16 v21, v17, v36, v40 op_sel_hi:[1,0,0]
	v_fma_mixhi_f16 v21, v17, v37, v41 op_sel:[1,0,0] op_sel_hi:[1,0,0]
	v_pk_max_f16 v21, v21, 0
	s_nop 1
	v_cndmask_b32_e32 v14, 0, v18, vcc
	v_cndmask_b32_e32 v15, 0, v19, vcc
	v_lshl_or_b32 v18, v57, 1, v69
	v_ashrrev_i32_e32 v19, 1, v22
	v_mad_u32_u24 v18, v18, 33, v19
	v_lshlrev_b32_e32 v19, 7, v18
	v_xor_b32_e32 v18, v18, v0
	v_lshlrev_b32_e32 v18, 4, v18
	v_and_b32_e32 v18, 0x70, v18
	v_cndmask_b32_e32 v16, 0, v20, vcc
	v_cndmask_b32_e32 v17, 0, v21, vcc
	v_add3_u32 v18, 0, v19, v18
	ds_write_b128 v18, v[14:17]
	v_add_u32_e32 v18, v56, v54
	v_fma_mixlo_f16 v14, v10, v26, v30 op_sel_hi:[1,0,0]
	v_fma_mixhi_f16 v14, v10, v27, v31 op_sel:[1,0,0] op_sel_hi:[1,0,0]
	v_pk_max_f16 v14, v14, 0
	v_add_u32_e32 v10, s27, v18
	v_max_u32_e32 v10, v55, v10
	v_fma_mixlo_f16 v15, v11, v28, v32 op_sel_hi:[1,0,0]
	v_fma_mixhi_f16 v15, v11, v29, v33 op_sel:[1,0,0] op_sel_hi:[1,0,0]
	v_pk_max_f16 v15, v15, 0
	v_cmp_gt_u32_e32 vcc, s10, v10
	v_fma_mixlo_f16 v16, v12, v34, v38 op_sel_hi:[1,0,0]
	v_fma_mixhi_f16 v16, v12, v35, v39 op_sel:[1,0,0] op_sel_hi:[1,0,0]
	v_pk_max_f16 v16, v16, 0
	v_fma_mixlo_f16 v17, v13, v36, v40 op_sel_hi:[1,0,0]
	v_fma_mixhi_f16 v17, v13, v37, v41 op_sel:[1,0,0] op_sel_hi:[1,0,0]
	v_pk_max_f16 v17, v17, 0
	s_nop 1
	v_cndmask_b32_e32 v10, 0, v14, vcc
	v_cndmask_b32_e32 v11, 0, v15, vcc
	v_lshl_or_b32 v14, v53, 1, v69
	v_ashrrev_i32_e32 v15, 1, v18
	v_mad_u32_u24 v14, v14, 33, v15
	v_lshlrev_b32_e32 v15, 7, v14
	v_xor_b32_e32 v14, v14, v0
	v_lshlrev_b32_e32 v14, 4, v14
	v_and_b32_e32 v14, 0x70, v14
	v_cndmask_b32_e32 v12, 0, v16, vcc
	v_cndmask_b32_e32 v13, 0, v17, vcc
	v_add3_u32 v14, 0, v15, v14
	v_cmp_gt_u32_e32 vcc, s6, v0
	ds_write_b128 v14, v[10:13]
	v_fma_mixlo_f16 v10, v6, v26, v30 op_sel_hi:[1,0,0]
	v_fma_mixhi_f16 v10, v6, v27, v31 op_sel:[1,0,0] op_sel_hi:[1,0,0]
	v_pk_max_f16 v10, v10, 0
	v_fma_mixlo_f16 v6, v7, v28, v32 op_sel_hi:[1,0,0]
	v_fma_mixhi_f16 v6, v7, v29, v33 op_sel:[1,0,0] op_sel_hi:[1,0,0]
	v_pk_max_f16 v6, v6, 0
	v_fma_mixlo_f16 v7, v8, v34, v38 op_sel_hi:[1,0,0]
	v_fma_mixhi_f16 v7, v8, v35, v39 op_sel:[1,0,0] op_sel_hi:[1,0,0]
	v_pk_max_f16 v7, v7, 0
	v_fma_mixlo_f16 v8, v9, v36, v40 op_sel_hi:[1,0,0]
	v_fma_mixhi_f16 v8, v9, v37, v41 op_sel:[1,0,0] op_sel_hi:[1,0,0]
	v_pk_max_f16 v8, v8, 0
	s_and_saveexec_b64 s[6:7], vcc
	s_cbranch_execz .LBB3_18
	v_mul_u32_u24_e32 v9, 0x3e1, v52
	v_lshrrev_b32_e32 v9, 16, v9
	s_movk_i32 s11, 0xffbe
	v_mad_i32_i24 v14, v9, s11, v52
	v_add_u32_e32 v11, s25, v9
	v_add_u32_e32 v12, s27, v14
	v_max_u32_e32 v11, v11, v12
	v_cmp_gt_u32_e32 vcc, s10, v11
	s_nop 1
	v_cndmask_b32_e32 v11, 0, v6, vcc
	v_cndmask_b32_e32 v12, 0, v7, vcc
	v_lshl_or_b32 v6, v9, 1, v69
	v_ashrrev_i32_e32 v7, 1, v14
	v_mad_u32_u24 v6, v6, 33, v7
	v_lshlrev_b32_e32 v7, 7, v6
	v_xor_b32_e32 v6, v6, v0
	v_lshlrev_b32_e32 v6, 4, v6
	v_and_b32_e32 v6, 0x70, v6
	v_cndmask_b32_e32 v10, 0, v10, vcc
	v_cndmask_b32_e32 v13, 0, v8, vcc
	v_add3_u32 v6, 0, v7, v6
	ds_write_b128 v6, v[10:13]

	.amdhsa_kernel _Z7kfinal3PKDF16_PKfS2_S2_PK15HIP_vector_typeIjLj4EES2_Pf
		.amdhsa_group_segment_fixed_size 0
		.amdhsa_private_segment_fixed_size 0
		.amdhsa_kernarg_size 56
		.amdhsa_user_sgpr_count 2
		.amdhsa_user_sgpr_dispatch_ptr 0
		.amdhsa_user_sgpr_queue_ptr 0
		.amdhsa_user_sgpr_kernarg_segment_ptr 1
		.amdhsa_user_sgpr_dispatch_id 0
		.amdhsa_user_sgpr_kernarg_preload_length 0
		.amdhsa_user_sgpr_kernarg_preload_offset 0
		.amdhsa_user_sgpr_private_segment_size 0
		.amdhsa_uses_dynamic_stack 0
		.amdhsa_enable_private_segment 0
		.amdhsa_system_sgpr_workgroup_id_x 1
		.amdhsa_system_sgpr_workgroup_id_y 0
		.amdhsa_system_sgpr_workgroup_id_z 0
		.amdhsa_system_sgpr_workgroup_info 0
		.amdhsa_system_vgpr_workitem_id 0
		.amdhsa_next_free_vgpr 217
		.amdhsa_next_free_sgpr 42
		.amdhsa_accum_offset 144
		.amdhsa_reserve_vcc 1
		.amdhsa_float_round_mode_32 0
		.amdhsa_float_round_mode_16_64 0
		.amdhsa_float_denorm_mode_32 3
		.amdhsa_float_denorm_mode_16_64 3
		.amdhsa_dx10_clamp 1
		.amdhsa_ieee_mode 1
		.amdhsa_fp16_overflow 0
		.amdhsa_tg_split 0
		.amdhsa_exception_fp_ieee_invalid_op 0
		.amdhsa_exception_fp_denorm_src 0
		.amdhsa_exception_fp_ieee_div_zero 0
		.amdhsa_exception_fp_ieee_overflow 0
		.amdhsa_exception_fp_ieee_underflow 0
		.amdhsa_exception_fp_ieee_inexact 0
		.amdhsa_exception_int_div_zero 0
	.end_amdhsa_kernel

amdhsa.kernels:
  - .agpr_count:     0
    .args:
      - .actual_access:  read_only
        .address_space:  global
        .offset:         0
        .size:           8
        .value_kind:     global_buffer
      - .actual_access:  read_only
        .address_space:  global
        .offset:         8
        .size:           8
        .value_kind:     global_buffer
      - .actual_access:  read_only
        .address_space:  global
        .offset:         16
        .size:           8
        .value_kind:     global_buffer
      - .actual_access:  read_only
        .address_space:  global
        .offset:         24
        .size:           8
        .value_kind:     global_buffer
      - .actual_access:  read_only
        .address_space:  global
        .offset:         32
        .size:           8
        .value_kind:     global_buffer
      - .actual_access:  read_only
        .address_space:  global
        .offset:         40
        .size:           8
        .value_kind:     global_buffer
      - .actual_access:  write_only
        .address_space:  global
        .offset:         48
        .size:           8
        .value_kind:     global_buffer
      - .actual_access:  write_only
        .address_space:  global
        .offset:         56
        .size:           8
        .value_kind:     global_buffer
      - .actual_access:  write_only
        .address_space:  global
        .offset:         64
        .size:           8
        .value_kind:     global_buffer
      - .actual_access:  write_only
        .address_space:  global
        .offset:         72
        .size:           8
        .value_kind:     global_buffer
    .group_segment_fixed_size: 12000
    .kernarg_segment_align: 8
    .kernarg_segment_size: 80
    .language:       OpenCL C
    .language_version:
      - 2
      - 0
    .max_flat_workgroup_size: 256
    .name:           _Z2k0PKfS0_S0_S0_S0_S0_PDF16_PfS1_S1_
    .private_segment_fixed_size: 0
    .sgpr_count:     24
    .sgpr_spill_count: 0
    .symbol:         _Z2k0PKfS0_S0_S0_S0_S0_PDF16_PfS1_S1_.kd
    .uniform_work_group_size: 1
    .uses_dynamic_stack: false
    .vgpr_count:     150
    .vgpr_spill_count: 0
    .wavefront_size: 64
  - .agpr_count:     16
    .args:
      - .actual_access:  read_only
        .address_space:  global
        .offset:         0
        .size:           8
        .value_kind:     global_buffer
      - .actual_access:  read_only
        .address_space:  global
        .offset:         8
        .size:           8
        .value_kind:     global_buffer
      - .actual_access:  read_only
        .address_space:  global
        .offset:         16
        .size:           8
        .value_kind:     global_buffer
      - .actual_access:  read_only
        .address_space:  global
        .offset:         24
        .size:           8
        .value_kind:     global_buffer
      - .actual_access:  read_only
        .address_space:  global
        .offset:         32
        .size:           8
        .value_kind:     global_buffer
      - .actual_access:  write_only
        .address_space:  global
        .offset:         40
        .size:           8
        .value_kind:     global_buffer
      - .actual_access:  write_only
        .address_space:  global
        .offset:         48
        .size:           8
        .value_kind:     global_buffer
    .group_segment_fixed_size: 14112
    .kernarg_segment_align: 8
    .kernarg_segment_size: 56
    .language:       OpenCL C
    .language_version:
      - 2
      - 0
    .max_flat_workgroup_size: 256
    .name:           _Z4khidPKDF16_PKfS2_S2_S0_PDF16_Pf
    .private_segment_fixed_size: 0
    .sgpr_count:     24
    .sgpr_spill_count: 0
    .symbol:         _Z4khidPKDF16_PKfS2_S2_S0_PDF16_Pf.kd
    .uniform_work_group_size: 1
    .uses_dynamic_stack: false
    .vgpr_count:     148
    .vgpr_spill_count: 0
    .wavefront_size: 64
  - .agpr_count:     144
    .args:
      - .actual_access:  read_only
        .address_space:  global
        .offset:         0
        .size:           8
        .value_kind:     global_buffer
      - .actual_access:  read_only
        .address_space:  global
        .offset:         8
        .size:           8
        .value_kind:     global_buffer
      - .actual_access:  read_only
        .address_space:  global
        .offset:         16
        .size:           8
        .value_kind:     global_buffer
      - .actual_access:  read_only
        .address_space:  global
        .offset:         24
        .size:           8
        .value_kind:     global_buffer
      - .address_space:  global
        .offset:         32
        .size:           8
        .value_kind:     global_buffer
      - .address_space:  global
        .offset:         40
        .size:           8
        .value_kind:     global_buffer
      - .address_space:  global
        .offset:         48
        .size:           8
        .value_kind:     global_buffer
    .group_segment_fixed_size: 0
    .kernarg_segment_align: 8
    .kernarg_segment_size: 56
    .language:       OpenCL C
    .language_version:
      - 2
      - 0
    .max_flat_workgroup_size: 256
    .name:           _Z6kfinalPKDF16_PKfS2_S2_PK15HIP_vector_typeIjLj4EES2_Pf
    .private_segment_fixed_size: 0
    .sgpr_count:     41
    .sgpr_spill_count: 0
    .symbol:         _Z6kfinalPKDF16_PKfS2_S2_PK15HIP_vector_typeIjLj4EES2_Pf.kd
    .uniform_work_group_size: 1
    .uses_dynamic_stack: false
    .vgpr_count:     400
    .vgpr_spill_count: 0
    .wavefront_size: 64
  - .agpr_count:     73
    .args:
      - .actual_access:  read_only
        .address_space:  global
        .offset:         0
        .size:           8
        .value_kind:     global_buffer
      - .actual_access:  read_only
        .address_space:  global
        .offset:         8
        .size:           8
        .value_kind:     global_buffer
      - .actual_access:  read_only
        .address_space:  global
        .offset:         16
        .size:           8
        .value_kind:     global_buffer
      - .actual_access:  read_only
        .address_space:  global
        .offset:         24
        .size:           8
        .value_kind:     global_buffer
      - .address_space:  global
        .offset:         32
        .size:           8
        .value_kind:     global_buffer
      - .address_space:  global
        .offset:         40
        .size:           8
        .value_kind:     global_buffer
      - .address_space:  global
        .offset:         48
        .size:           8
        .value_kind:     global_buffer
    .group_segment_fixed_size: 0
    .kernarg_segment_align: 8
    .kernarg_segment_size: 56
    .language:       OpenCL C
    .language_version:
      - 2
      - 0
    .max_flat_workgroup_size: 512
    .name:           _Z7kfinal3PKDF16_PKfS2_S2_PK15HIP_vector_typeIjLj4EES2_Pf
    .private_segment_fixed_size: 0
    .sgpr_count:     48
    .sgpr_spill_count: 0
    .symbol:         _Z7kfinal3PKDF16_PKfS2_S2_PK15HIP_vector_typeIjLj4EES2_Pf.kd
    .uniform_work_group_size: 1
    .uses_dynamic_stack: false
    .vgpr_count:     217
    .vgpr_spill_count: 0
    .wavefront_size: 64
